# speedup vs baseline: 1.0150x; 1.0150x over previous
.LBB1_37:
	v_or_b32_e32 v12, s6, v1
	v_max_f32_e32 v15, v10, v10
	v_mul_u32_u24_e32 v10, 44, v12
	v_max_f32_e32 v13, v11, v11
	v_max_f32_e32 v14, v9, v9
	v_max_f32_e32 v16, v7, v7
	v_max_f32_e32 v17, v8, v8
	v_max_f32_e32 v18, v6, v6
	v_max_f32_e32 v19, v4, v4
	v_max_f32_e32 v20, v5, v5
	v_max_f32_e32 v21, v2, v2
	v_max_f32_e32 v22, v3, v3
	ds_read2_b32 v[2:3], v10 offset0:6 offset1:7
	ds_read2_b32 v[4:5], v10 offset0:2 offset1:3
	ds_read2_b32 v[6:7], v10 offset0:4 offset1:5
	ds_read2_b32 v[8:9], v10 offset0:8 offset1:9
	ds_read2_b32 v[10:11], v10 offset1:1
	s_waitcnt lgkmcnt(4)
	v_max_f32_e32 v3, v3, v3
	v_max_f32_e32 v2, v2, v2
	s_waitcnt lgkmcnt(3)
	v_max_f32_e32 v5, v5, v5
	s_waitcnt lgkmcnt(1)
	v_max_f32_e32 v9, v9, v9
	v_max_f32_e32 v8, v8, v8
	v_max_f32_e32 v7, v7, v7
	s_waitcnt lgkmcnt(0)
	v_max_f32_e32 v11, v11, v11
	v_max_f32_e32 v4, v4, v4
	v_max_f32_e32 v6, v6, v6
	v_max_f32_e32 v10, v10, v10
	v_min_f32_e32 v3, v13, v3
	v_min_f32_e32 v9, v17, v9
	v_min_f32_e32 v2, v18, v2
	v_min_f32_e32 v8, v22, v8
	v_max_f32_e32 v12, v15, v5
	v_max_f32_e32 v13, v16, v7
	v_max_f32_e32 v17, v20, v4
	v_max_f32_e32 v18, v21, v6
	v_min_f32_e32 v5, v15, v5
	v_min_f32_e32 v7, v16, v7
	v_min_f32_e32 v4, v20, v4
	v_min_f32_e32 v6, v21, v6
	v_max_f32_e32 v15, v14, v3
	v_max_f32_e32 v16, v9, v11
	v_max_f32_e32 v20, v19, v2
	v_max_f32_e32 v21, v8, v10
	v_min_f32_e32 v3, v14, v3
	v_min_f32_e32 v9, v9, v11
	v_min_f32_e32 v2, v19, v2
	v_min_f32_e32 v8, v8, v10
	v_min_f32_e32 v10, v3, v5
	v_min_f32_e32 v11, v7, v9
	v_min_f32_e32 v14, v2, v4
	v_min_f32_e32 v19, v6, v8
	v_max_f32_e32 v3, v3, v5
	v_max_f32_e32 v5, v7, v9
	v_max_f32_e32 v2, v2, v4
	v_max_f32_e32 v4, v6, v8
	v_min_f32_e32 v6, v13, v16
	v_min_f32_e32 v7, v18, v21
	v_min_f32_e32 v8, v10, v11
	v_min_f32_e32 v13, v14, v19
	v_max_f32_e32 v10, v10, v11
	v_max_f32_e32 v11, v14, v19
	v_min_f32_e32 v14, v3, v5
	v_min_f32_e32 v16, v2, v4
	v_max_f32_e32 v3, v3, v5
	v_max_f32_e32 v18, v2, v4
	v_min3_f32 v6, v15, v12, v6
	v_min3_f32 v12, v20, v17, v7
	s_movk_i32 s6, 0x80
	s_and_b64 vcc, exec, s[4:5]
	s_mov_b64 s[4:5], 0
	v_min_f32_e32 v9, v8, v13
	v_max_f32_e32 v4, v8, v13
	v_min_f32_e32 v7, v10, v11
	v_max_f32_e32 v2, v10, v11
	v_min_f32_e32 v10, v14, v16
	v_max_f32_e32 v5, v14, v16
	v_min_f32_e32 v8, v3, v18
	v_max_f32_e32 v3, v3, v18
	v_min_f32_e32 v11, v6, v12
	v_max_f32_e32 v6, v6, v12
	s_cbranch_vccnz .LBB1_37
	v_or_b32_e32 v12, s33, v1
	s_movk_i32 s4, 0x400
	v_mov_b32_e32 v13, 0x1e0000
	v_cmp_gt_i32_e32 vcc, s4, v12
	s_lshl_b32 s4, s8, 2
	v_mov_b32_e32 v15, 0
	v_cndmask_b32_e64 v14, v13, 0, vcc
	s_add_i32 s4, s4, s76
	s_mov_b32 s5, 0
	v_lshl_add_u64 v[16:17], s[70:71], 0, v[14:15]
	s_mul_i32 s4, s4, 12
	v_cndmask_b32_e64 v14, 13, 10, vcc
	v_lshlrev_b64 v[18:19], v14, s[4:5]
	v_lshl_add_u64 v[16:17], v[18:19], 2, v[16:17]
	v_ashrrev_i32_e32 v13, 31, v12
	v_lshl_add_u64 v[12:13], v[12:13], 2, v[16:17]
	v_lshlrev_b64 v[16:17], v14, 1
	v_lshl_add_u64 v[16:17], v[16:17], 2, v[12:13]
	global_store_dword v[16:17], v4, off sc0 sc1
	v_lshlrev_b64 v[16:17], v14, 2
	v_lshl_add_u64 v[16:17], v[16:17], 2, v[12:13]
	global_store_dword v[16:17], v7, off sc0 sc1
	v_lshlrev_b64 v[16:17], v14, 3
	v_lshl_add_u64 v[16:17], v[16:17], 2, v[12:13]
	global_store_dword v[16:17], v2, off sc0 sc1
	v_lshlrev_b64 v[16:17], v14, 4
	v_lshl_add_u64 v[16:17], v[16:17], 2, v[12:13]
	global_store_dword v[16:17], v10, off sc0 sc1
	v_lshlrev_b64 v[16:17], v14, 5
	v_lshl_add_u64 v[16:17], v[16:17], 2, v[12:13]
	global_store_dword v[16:17], v5, off sc0 sc1
	v_lshlrev_b64 v[4:5], v14, 6
	v_lshl_add_u64 v[4:5], v[4:5], 2, v[12:13]
	global_store_dword v[4:5], v8, off sc0 sc1
	v_lshlrev_b64 v[4:5], v14, 7
	v_lshl_add_u64 v[4:5], v[4:5], 2, v[12:13]
	global_store_dword v[4:5], v3, off sc0 sc1
	v_lshlrev_b64 v[2:3], v14, 8
	v_lshl_add_u64 v[2:3], v[2:3], 2, v[12:13]
	global_store_dword v[2:3], v11, off sc0 sc1
	v_lshlrev_b64 v[2:3], v14, 9
	v_lshl_add_u64 v[2:3], v[2:3], 2, v[12:13]
	global_store_dword v[2:3], v6, off sc0 sc1
	v_mov_b32_e32 v2, 0x58000
	v_mov_b32_e32 v3, 0xb000
	v_cndmask_b32_e32 v14, v2, v3, vcc
	v_lshl_add_u64 v[2:3], v[12:13], 0, v[14:15]
	global_store_dword v[12:13], v9, off sc0 sc1
	global_store_dword v[2:3], v116, off sc0 sc1
